# baseline (speedup 1.0000x reference)
.Lmypd:
	s_waitcnt vmcnt(15)
	v_mov_b32_dpp v0, v4 row_shr:1 row_mask:0xf bank_mask:0xf
	v_mov_b32_dpp v1, v5 row_shr:1 row_mask:0xf bank_mask:0xf
	v_mov_b32_dpp v6, v2 row_shl:1 row_mask:0xf bank_mask:0xf
	v_mov_b32_dpp v7, v3 row_shl:1 row_mask:0xf bank_mask:0xf
	v_pk_mul_f32 v[2:3], v[2:3], s[32:33]
	v_pk_mul_f32 v[4:5], v[4:5], s[32:33]
	v_cndmask_b32_e64 v1, v1, v0, vcc
	v_cndmask_b32_e64 v6, v6, v7, s[16:17]
	v_pk_mul_f32 v[0:1], v[0:1], s[32:33]
	v_pk_mul_f32 v[6:7], v[6:7], s[32:33]
	s_waitcnt vmcnt(15)
	s_nop 0
	v_mov_b32_dpp v8, v12 row_shr:1 row_mask:0xf bank_mask:0xf
	v_mov_b32_dpp v9, v13 row_shr:1 row_mask:0xf bank_mask:0xf
	v_mov_b32_dpp v14, v10 row_shl:1 row_mask:0xf bank_mask:0xf
	v_mov_b32_dpp v15, v11 row_shl:1 row_mask:0xf bank_mask:0xf
	v_pk_mul_f32 v[10:11], v[10:11], s[32:33]
	v_pk_mul_f32 v[12:13], v[12:13], s[32:33]
	v_cndmask_b32_e64 v9, v9, v8, vcc
	v_cndmask_b32_e64 v14, v14, v15, s[16:17]
	v_pk_mul_f32 v[8:9], v[8:9], s[32:33]
	v_pk_mul_f32 v[14:15], v[14:15], s[32:33]
	s_waitcnt vmcnt(15)
	s_nop 0
	v_mov_b32_dpp v16, v20 row_shr:1 row_mask:0xf bank_mask:0xf
	v_mov_b32_dpp v17, v21 row_shr:1 row_mask:0xf bank_mask:0xf
	v_mov_b32_dpp v22, v18 row_shl:1 row_mask:0xf bank_mask:0xf
	v_mov_b32_dpp v23, v19 row_shl:1 row_mask:0xf bank_mask:0xf
	v_pk_mul_f32 v[18:19], v[18:19], s[32:33]
	v_pk_mul_f32 v[20:21], v[20:21], s[32:33]
	v_cndmask_b32_e64 v17, v17, v16, vcc
	v_cndmask_b32_e64 v22, v22, v23, s[16:17]
	v_pk_mul_f32 v[68:69], v[18:19], s[30:31]
	v_pk_mul_f32 v[70:71], v[20:21], s[30:31]
	v_pk_mul_f32 v[16:17], v[16:17], s[32:33]
	v_pk_mul_f32 v[22:23], v[22:23], s[32:33]
	v_pk_add_f32 v[96:97], v[18:19], v[0:1] neg_lo:[0,1] neg_hi:[0,1]
	v_pk_add_f32 v[98:99], v[18:19], v[2:3] neg_lo:[0,1] neg_hi:[0,1]
	v_pk_add_f32 v[100:101], v[20:21], v[2:3] neg_lo:[0,1] neg_hi:[0,1]
	v_pk_add_f32 v[102:103], v[18:19], v[4:5] neg_lo:[0,1] neg_hi:[0,1]
	v_pk_fma_f32 v[96:97], v[96:97], v[96:97], s[28:29] neg_lo:[1,0,0] neg_hi:[1,0,0]
	v_pk_fma_f32 v[98:99], v[98:99], v[98:99], s[22:23] neg_lo:[1,0,0] neg_hi:[1,0,0]
	v_pk_fma_f32 v[100:101], v[100:101], v[100:101], s[28:29] neg_lo:[1,0,0] neg_hi:[1,0,0]
	v_pk_fma_f32 v[102:103], v[102:103], v[102:103], s[28:29] neg_lo:[1,0,0] neg_hi:[1,0,0]
	v_exp_f32_e32 v96, v96
	v_exp_f32_e32 v97, v97
	v_exp_f32_e32 v98, v98
	v_exp_f32_e32 v99, v99
	v_exp_f32_e32 v100, v100
	v_exp_f32_e32 v101, v101
	v_exp_f32_e32 v102, v102
	v_exp_f32_e32 v103, v103
	v_pk_add_f32 v[104:105], v[20:21], v[4:5] neg_lo:[0,1] neg_hi:[0,1]
	v_pk_add_f32 v[106:107], v[20:21], v[6:7] neg_lo:[0,1] neg_hi:[0,1]
	v_pk_add_f32 v[108:109], v[18:19], v[2:3] op_sel:[1,0] op_sel_hi:[0,1] neg_lo:[0,1] neg_hi:[0,1]
	v_pk_add_f32 v[110:111], v[20:21], v[4:5] op_sel:[1,0] op_sel_hi:[0,1] neg_lo:[0,1] neg_hi:[0,1]
	v_pk_fma_f32 v[104:105], v[104:105], v[104:105], s[22:23] neg_lo:[1,0,0] neg_hi:[1,0,0]
	v_pk_fma_f32 v[106:107], v[106:107], v[106:107], s[28:29] neg_lo:[1,0,0] neg_hi:[1,0,0]
	v_pk_fma_f32 v[108:109], v[108:109], v[108:109], s[26:27] neg_lo:[1,0,0] neg_hi:[1,0,0]
	v_pk_fma_f32 v[110:111], v[110:111], v[110:111], s[26:27] neg_lo:[1,0,0] neg_hi:[1,0,0]
	v_exp_f32_e32 v104, v104
	v_exp_f32_e32 v105, v105
	v_exp_f32_e32 v106, v106
	v_exp_f32_e32 v107, v107
	v_exp_f32_e32 v108, v108
	v_exp_f32_e32 v109, v109
	v_exp_f32_e32 v110, v110
	v_exp_f32_e32 v111, v111
	v_pk_add_f32 v[64:65], s[30:31], v[96:97]
	v_pk_fma_f32 v[68:69], v[96:97], v[0:1], v[68:69]
	v_pk_add_f32 v[66:67], s[30:31], v[100:101]
	v_pk_add_f32 v[64:65], v[64:65], v[98:99]
	v_pk_fma_f32 v[68:69], v[98:99], v[2:3], v[68:69]
	v_pk_fma_f32 v[70:71], v[100:101], v[2:3], v[70:71]
	v_pk_add_f32 v[64:65], v[64:65], v[102:103]
	v_pk_fma_f32 v[68:69], v[102:103], v[4:5], v[68:69]
	v_pk_add_f32 v[96:97], v[18:19], v[8:9] neg_lo:[0,1] neg_hi:[0,1]
	v_pk_add_f32 v[98:99], v[18:19], v[10:11] neg_lo:[0,1] neg_hi:[0,1]
	v_pk_add_f32 v[100:101], v[20:21], v[10:11] neg_lo:[0,1] neg_hi:[0,1]
	v_pk_add_f32 v[102:103], v[18:19], v[12:13] neg_lo:[0,1] neg_hi:[0,1]
	v_pk_fma_f32 v[96:97], v[96:97], v[96:97], s[26:27] neg_lo:[1,0,0] neg_hi:[1,0,0]
	v_pk_fma_f32 v[98:99], v[98:99], v[98:99], s[20:21] neg_lo:[1,0,0] neg_hi:[1,0,0]
	v_pk_fma_f32 v[100:101], v[100:101], v[100:101], s[26:27] neg_lo:[1,0,0] neg_hi:[1,0,0]
	v_pk_fma_f32 v[102:103], v[102:103], v[102:103], s[26:27] neg_lo:[1,0,0] neg_hi:[1,0,0]
	v_exp_f32_e32 v96, v96
	v_exp_f32_e32 v97, v97
	v_exp_f32_e32 v98, v98
	v_exp_f32_e32 v99, v99
	v_exp_f32_e32 v100, v100
	v_exp_f32_e32 v101, v101
	v_exp_f32_e32 v102, v102
	v_exp_f32_e32 v103, v103
	v_pk_add_f32 v[66:67], v[66:67], v[104:105]
	v_pk_fma_f32 v[70:71], v[104:105], v[4:5], v[70:71]
	v_pk_add_f32 v[64:65], v[64:65], v[108:109] op_sel:[0,1] op_sel_hi:[1,0]
	v_pk_add_f32 v[66:67], v[66:67], v[106:107]
	v_pk_fma_f32 v[70:71], v[106:107], v[6:7], v[70:71]
	v_pk_fma_f32 v[68:69], v[108:109], v[2:3], v[68:69] op_sel:[1,1,0] op_sel_hi:[0,0,1]
	v_pk_add_f32 v[66:67], v[66:67], v[110:111] op_sel:[0,1] op_sel_hi:[1,0]
	v_pk_fma_f32 v[70:71], v[110:111], v[4:5], v[70:71] op_sel:[1,1,0] op_sel_hi:[0,0,1]
	v_pk_add_f32 v[104:105], v[20:21], v[12:13] neg_lo:[0,1] neg_hi:[0,1]
	v_pk_add_f32 v[106:107], v[20:21], v[14:15] neg_lo:[0,1] neg_hi:[0,1]
	v_pk_add_f32 v[108:109], v[18:19], v[10:11] op_sel:[1,0] op_sel_hi:[0,1] neg_lo:[0,1] neg_hi:[0,1]
	v_pk_add_f32 v[110:111], v[20:21], v[12:13] op_sel:[1,0] op_sel_hi:[0,1] neg_lo:[0,1] neg_hi:[0,1]
	v_pk_fma_f32 v[104:105], v[104:105], v[104:105], s[20:21] neg_lo:[1,0,0] neg_hi:[1,0,0]
	v_pk_fma_f32 v[106:107], v[106:107], v[106:107], s[26:27] neg_lo:[1,0,0] neg_hi:[1,0,0]
	v_pk_fma_f32 v[108:109], v[108:109], v[108:109], s[24:25] neg_lo:[1,0,0] neg_hi:[1,0,0]
	v_pk_fma_f32 v[110:111], v[110:111], v[110:111], s[24:25] neg_lo:[1,0,0] neg_hi:[1,0,0]
	v_exp_f32_e32 v104, v104
	v_exp_f32_e32 v105, v105
	v_exp_f32_e32 v106, v106
	v_exp_f32_e32 v107, v107
	v_exp_f32_e32 v108, v108
	v_exp_f32_e32 v109, v109
	v_exp_f32_e32 v110, v110
	v_exp_f32_e32 v111, v111
	v_pk_add_f32 v[64:65], v[64:65], v[96:97]
	v_pk_fma_f32 v[68:69], v[96:97], v[8:9], v[68:69]
	v_pk_add_f32 v[66:67], v[66:67], v[100:101]
	v_pk_add_f32 v[64:65], v[64:65], v[98:99]
	v_pk_fma_f32 v[68:69], v[98:99], v[10:11], v[68:69]
	v_pk_fma_f32 v[70:71], v[100:101], v[10:11], v[70:71]
	v_pk_add_f32 v[64:65], v[64:65], v[102:103]
	v_pk_fma_f32 v[68:69], v[102:103], v[12:13], v[68:69]
	v_pk_add_f32 v[96:97], v[18:19], v[16:17] neg_lo:[0,1] neg_hi:[0,1]
	v_pk_add_f32 v[98:99], v[20:21], v[18:19] neg_lo:[0,1] neg_hi:[0,1]
	v_pk_add_f32 v[100:101], v[22:23], v[20:21] neg_lo:[0,1] neg_hi:[0,1]
	v_pk_fma_f32 v[96:97], v[96:97], v[96:97], s[22:23] neg_lo:[1,0,0] neg_hi:[1,0,0]
	v_pk_fma_f32 v[98:99], v[98:99], v[98:99], s[22:23] neg_lo:[1,0,0] neg_hi:[1,0,0]
	v_pk_fma_f32 v[100:101], v[100:101], v[100:101], s[22:23] neg_lo:[1,0,0] neg_hi:[1,0,0]
	v_exp_f32_e32 v96, v96
	v_exp_f32_e32 v97, v97
	v_exp_f32_e32 v98, v98
	v_exp_f32_e32 v99, v99
	v_exp_f32_e32 v100, v100
	v_exp_f32_e32 v101, v101
	v_pk_add_f32 v[66:67], v[66:67], v[104:105]
	v_pk_fma_f32 v[70:71], v[104:105], v[12:13], v[70:71]
	v_pk_add_f32 v[64:65], v[64:65], v[108:109] op_sel:[0,1] op_sel_hi:[1,0]
	v_pk_add_f32 v[66:67], v[66:67], v[106:107]
	v_pk_fma_f32 v[70:71], v[106:107], v[14:15], v[70:71]
	v_pk_fma_f32 v[68:69], v[108:109], v[10:11], v[68:69] op_sel:[1,1,0] op_sel_hi:[0,0,1]
	v_pk_add_f32 v[66:67], v[66:67], v[110:111] op_sel:[0,1] op_sel_hi:[1,0]
	v_pk_fma_f32 v[70:71], v[110:111], v[12:13], v[70:71] op_sel:[1,1,0] op_sel_hi:[0,0,1]
	v_sub_f32_e32 v104, v18, v1
	v_sub_f32_e32 v106, v20, v3
	v_sub_f32_e32 v108, v19, v4
	v_sub_f32_e32 v110, v21, v6
	v_sub_f32_e32 v105, v18, v9
	v_sub_f32_e32 v107, v20, v11
	v_sub_f32_e32 v109, v19, v12
	v_sub_f32_e32 v111, v21, v14
	v_fma_f32 v104, -v104, v104, s26
	v_fma_f32 v106, -v106, v106, s26
	v_fma_f32 v108, -v108, v108, s26
	v_fma_f32 v110, -v110, v110, s26
	v_fma_f32 v105, -v105, v105, s24
	v_fma_f32 v107, -v107, v107, s24
	v_fma_f32 v109, -v109, v109, s24
	v_fma_f32 v111, -v111, v111, s24
	v_exp_f32_e32 v104, v104
	v_exp_f32_e32 v106, v106
	v_exp_f32_e32 v108, v108
	v_exp_f32_e32 v110, v110
	v_exp_f32_e32 v105, v105
	v_exp_f32_e32 v107, v107
	v_exp_f32_e32 v109, v109
	v_exp_f32_e32 v111, v111
	v_pk_add_f32 v[64:65], v[64:65], v[96:97]
	v_pk_fma_f32 v[68:69], v[96:97], v[16:17], v[68:69]
	v_pk_add_f32 v[66:67], v[66:67], v[98:99]
	v_pk_add_f32 v[64:65], v[64:65], v[98:99]
	v_pk_fma_f32 v[68:69], v[98:99], v[20:21], v[68:69]
	v_pk_fma_f32 v[70:71], v[98:99], v[18:19], v[70:71]
	v_pk_add_f32 v[66:67], v[66:67], v[100:101]
	v_pk_fma_f32 v[70:71], v[100:101], v[22:23], v[70:71]
	v_sub_f32_e32 v100, v18, v17
	v_sub_f32_e32 v96, v19, v18
	v_sub_f32_e32 v102, v20, v19
	v_sub_f32_e32 v98, v21, v20
	v_sub_f32_e64 v97, v22, v21
	v_fma_f32 v100, -v100, v100, s20
	v_fma_f32 v96, -v96, v96, s20
	v_fma_f32 v102, -v102, v102, s20
	v_fma_f32 v98, -v98, v98, s20
	v_fma_f32 v97, -v97, v97, s20
	v_exp_f32_e32 v100, v100
	v_exp_f32_e32 v96, v96
	v_exp_f32_e32 v102, v102
	v_exp_f32_e32 v98, v98
	v_exp_f32_e32 v97, v97
	v_add_f32_e32 v64, v64, v104
	v_fmac_f32_e32 v68, v104, v1
	v_add_f32_e32 v66, v66, v106
	v_fmac_f32_e32 v70, v106, v3
	v_add_f32_e32 v65, v65, v108
	v_fmac_f32_e32 v69, v108, v4
	v_add_f32_e32 v67, v67, v110
	v_fmac_f32_e32 v71, v110, v6
	v_add_f32_e32 v64, v64, v105
	v_fmac_f32_e32 v68, v105, v9
	v_add_f32_e32 v66, v66, v107
	v_fmac_f32_e32 v70, v107, v11
	v_add_f32_e32 v65, v65, v109
	v_fmac_f32_e32 v69, v109, v12
	v_add_f32_e32 v67, v67, v111
	v_fmac_f32_e32 v71, v111, v14
	v_add_f32_e32 v64, v64, v100
	v_fmac_f32_e32 v68, v100, v17
	v_add_f32_e32 v65, v65, v102
	v_fmac_f32_e32 v69, v102, v20
	v_add_f32_e32 v66, v66, v102
	v_fmac_f32_e32 v70, v102, v19
	v_add_f32_e32 v67, v67, v97
	v_fmac_f32_e64 v71, v97, v22
	v_pk_add_f32 v[64:65], v[64:65], v[96:97] op_sel_hi:[1,0]
	v_pk_fma_f32 v[68:69], v[96:97], v[18:19], v[68:69] op_sel:[0,1,0] op_sel_hi:[0,0,1]
	v_pk_add_f32 v[66:67], v[66:67], v[98:99] op_sel_hi:[1,0]
	v_pk_fma_f32 v[70:71], v[98:99], v[20:21], v[70:71] op_sel:[0,1,0] op_sel_hi:[0,0,1]
	s_waitcnt vmcnt(12)
	s_nop 0
	v_mov_b32_dpp v24, v28 row_shr:1 row_mask:0xf bank_mask:0xf
	v_mov_b32_dpp v25, v29 row_shr:1 row_mask:0xf bank_mask:0xf
	v_mov_b32_dpp v30, v26 row_shl:1 row_mask:0xf bank_mask:0xf
	v_mov_b32_dpp v31, v27 row_shl:1 row_mask:0xf bank_mask:0xf
	v_pk_mul_f32 v[26:27], v[26:27], s[32:33]
	v_pk_mul_f32 v[28:29], v[28:29], s[32:33]
	v_cndmask_b32_e64 v25, v25, v24, vcc
	v_cndmask_b32_e64 v30, v30, v31, s[16:17]
	v_pk_mul_f32 v[76:77], v[26:27], s[30:31]
	v_pk_mul_f32 v[78:79], v[28:29], s[30:31]
	v_pk_mul_f32 v[24:25], v[24:25], s[32:33]
	v_pk_mul_f32 v[30:31], v[30:31], s[32:33]
	v_pk_add_f32 v[96:97], v[26:27], v[8:9] neg_lo:[0,1] neg_hi:[0,1]
	v_pk_add_f32 v[98:99], v[26:27], v[10:11] neg_lo:[0,1] neg_hi:[0,1]
	v_pk_add_f32 v[100:101], v[28:29], v[10:11] neg_lo:[0,1] neg_hi:[0,1]
	v_pk_add_f32 v[102:103], v[26:27], v[12:13] neg_lo:[0,1] neg_hi:[0,1]
	v_pk_fma_f32 v[96:97], v[96:97], v[96:97], s[28:29] neg_lo:[1,0,0] neg_hi:[1,0,0]
	v_pk_fma_f32 v[98:99], v[98:99], v[98:99], s[22:23] neg_lo:[1,0,0] neg_hi:[1,0,0]
	v_pk_fma_f32 v[100:101], v[100:101], v[100:101], s[28:29] neg_lo:[1,0,0] neg_hi:[1,0,0]
	v_pk_fma_f32 v[102:103], v[102:103], v[102:103], s[28:29] neg_lo:[1,0,0] neg_hi:[1,0,0]
	v_exp_f32_e32 v96, v96
	v_exp_f32_e32 v97, v97
	v_exp_f32_e32 v98, v98
	v_exp_f32_e32 v99, v99
	v_exp_f32_e32 v100, v100
	v_exp_f32_e32 v101, v101
	v_exp_f32_e32 v102, v102
	v_exp_f32_e32 v103, v103
	v_pk_add_f32 v[104:105], v[28:29], v[12:13] neg_lo:[0,1] neg_hi:[0,1]
	v_pk_add_f32 v[106:107], v[28:29], v[14:15] neg_lo:[0,1] neg_hi:[0,1]
	v_pk_add_f32 v[108:109], v[26:27], v[10:11] op_sel:[1,0] op_sel_hi:[0,1] neg_lo:[0,1] neg_hi:[0,1]
	v_pk_add_f32 v[110:111], v[28:29], v[12:13] op_sel:[1,0] op_sel_hi:[0,1] neg_lo:[0,1] neg_hi:[0,1]
	v_pk_fma_f32 v[104:105], v[104:105], v[104:105], s[22:23] neg_lo:[1,0,0] neg_hi:[1,0,0]
	v_pk_fma_f32 v[106:107], v[106:107], v[106:107], s[28:29] neg_lo:[1,0,0] neg_hi:[1,0,0]
	v_pk_fma_f32 v[108:109], v[108:109], v[108:109], s[26:27] neg_lo:[1,0,0] neg_hi:[1,0,0]
	v_pk_fma_f32 v[110:111], v[110:111], v[110:111], s[26:27] neg_lo:[1,0,0] neg_hi:[1,0,0]
	v_exp_f32_e32 v104, v104
	v_exp_f32_e32 v105, v105
	v_exp_f32_e32 v106, v106
	v_exp_f32_e32 v107, v107
	v_exp_f32_e32 v108, v108
	v_exp_f32_e32 v109, v109
	v_exp_f32_e32 v110, v110
	v_exp_f32_e32 v111, v111
	v_pk_add_f32 v[72:73], s[30:31], v[96:97]
	v_pk_fma_f32 v[76:77], v[96:97], v[8:9], v[76:77]
	v_pk_add_f32 v[74:75], s[30:31], v[100:101]
	v_pk_add_f32 v[72:73], v[72:73], v[98:99]
	v_pk_fma_f32 v[76:77], v[98:99], v[10:11], v[76:77]
	v_pk_fma_f32 v[78:79], v[100:101], v[10:11], v[78:79]
	v_pk_add_f32 v[72:73], v[72:73], v[102:103]
	v_pk_fma_f32 v[76:77], v[102:103], v[12:13], v[76:77]
	v_pk_add_f32 v[96:97], v[26:27], v[16:17] neg_lo:[0,1] neg_hi:[0,1]
	v_pk_add_f32 v[98:99], v[24:25], v[18:19] neg_lo:[0,1] neg_hi:[0,1]
	v_pk_add_f32 v[100:101], v[26:27], v[18:19] neg_lo:[0,1] neg_hi:[0,1]
	v_pk_add_f32 v[102:103], v[28:29], v[18:19] neg_lo:[0,1] neg_hi:[0,1]
	v_pk_fma_f32 v[96:97], v[96:97], v[96:97], s[26:27] neg_lo:[1,0,0] neg_hi:[1,0,0]
	v_pk_fma_f32 v[98:99], v[98:99], v[98:99], s[26:27] neg_lo:[1,0,0] neg_hi:[1,0,0]
	v_pk_fma_f32 v[100:101], v[100:101], v[100:101], s[20:21] neg_lo:[1,0,0] neg_hi:[1,0,0]
	v_pk_fma_f32 v[102:103], v[102:103], v[102:103], s[26:27] neg_lo:[1,0,0] neg_hi:[1,0,0]
	v_exp_f32_e32 v96, v96
	v_exp_f32_e32 v97, v97
	v_exp_f32_e32 v98, v98
	v_exp_f32_e32 v99, v99
	v_exp_f32_e32 v100, v100
	v_exp_f32_e32 v101, v101
	v_exp_f32_e32 v102, v102
	v_exp_f32_e32 v103, v103
	v_pk_add_f32 v[74:75], v[74:75], v[104:105]
	v_pk_fma_f32 v[78:79], v[104:105], v[12:13], v[78:79]
	v_pk_add_f32 v[72:73], v[72:73], v[108:109] op_sel:[0,1] op_sel_hi:[1,0]
	v_pk_add_f32 v[74:75], v[74:75], v[106:107]
	v_pk_fma_f32 v[78:79], v[106:107], v[14:15], v[78:79]
	v_pk_fma_f32 v[76:77], v[108:109], v[10:11], v[76:77] op_sel:[1,1,0] op_sel_hi:[0,0,1]
	v_pk_add_f32 v[74:75], v[74:75], v[110:111] op_sel:[0,1] op_sel_hi:[1,0]
	v_pk_fma_f32 v[78:79], v[110:111], v[12:13], v[78:79] op_sel:[1,1,0] op_sel_hi:[0,0,1]
	v_pk_add_f32 v[104:105], v[26:27], v[20:21] neg_lo:[0,1] neg_hi:[0,1]
	v_pk_add_f32 v[106:107], v[28:29], v[20:21] neg_lo:[0,1] neg_hi:[0,1]
	v_pk_add_f32 v[108:109], v[30:31], v[20:21] neg_lo:[0,1] neg_hi:[0,1]
	v_pk_add_f32 v[110:111], v[28:29], v[22:23] neg_lo:[0,1] neg_hi:[0,1]
	v_pk_fma_f32 v[104:105], v[104:105], v[104:105], s[26:27] neg_lo:[1,0,0] neg_hi:[1,0,0]
	v_pk_fma_f32 v[106:107], v[106:107], v[106:107], s[20:21] neg_lo:[1,0,0] neg_hi:[1,0,0]
	v_pk_fma_f32 v[108:109], v[108:109], v[108:109], s[26:27] neg_lo:[1,0,0] neg_hi:[1,0,0]
	v_pk_fma_f32 v[110:111], v[110:111], v[110:111], s[26:27] neg_lo:[1,0,0] neg_hi:[1,0,0]
	v_exp_f32_e32 v104, v104
	v_exp_f32_e32 v105, v105
	v_exp_f32_e32 v106, v106
	v_exp_f32_e32 v107, v107
	v_exp_f32_e32 v108, v108
	v_exp_f32_e32 v109, v109
	v_exp_f32_e32 v110, v110
	v_exp_f32_e32 v111, v111
	v_pk_add_f32 v[72:73], v[72:73], v[96:97]
	v_pk_fma_f32 v[76:77], v[96:97], v[16:17], v[76:77]
	v_pk_add_f32 v[64:65], v[64:65], v[98:99]
	v_pk_fma_f32 v[68:69], v[98:99], v[24:25], v[68:69]
	v_pk_add_f32 v[72:73], v[72:73], v[100:101]
	v_pk_add_f32 v[64:65], v[64:65], v[100:101]
	v_pk_fma_f32 v[68:69], v[100:101], v[26:27], v[68:69]
	v_pk_fma_f32 v[76:77], v[100:101], v[18:19], v[76:77]
	v_pk_add_f32 v[64:65], v[64:65], v[102:103]
	v_pk_fma_f32 v[68:69], v[102:103], v[28:29], v[68:69]
	v_pk_add_f32 v[74:75], v[74:75], v[102:103]
	v_pk_fma_f32 v[78:79], v[102:103], v[18:19], v[78:79]
	v_pk_add_f32 v[96:97], v[26:27], v[18:19] op_sel:[1,0] op_sel_hi:[0,1] neg_lo:[0,1] neg_hi:[0,1]
	v_pk_add_f32 v[98:99], v[28:29], v[20:21] op_sel:[1,0] op_sel_hi:[0,1] neg_lo:[0,1] neg_hi:[0,1]
	v_pk_add_f32 v[100:101], v[26:27], v[24:25] neg_lo:[0,1] neg_hi:[0,1]
	v_pk_add_f32 v[102:103], v[28:29], v[26:27] neg_lo:[0,1] neg_hi:[0,1]
	v_pk_fma_f32 v[96:97], v[96:97], v[96:97], s[24:25] neg_lo:[1,0,0] neg_hi:[1,0,0]
	v_pk_fma_f32 v[98:99], v[98:99], v[98:99], s[24:25] neg_lo:[1,0,0] neg_hi:[1,0,0]
	v_pk_fma_f32 v[100:101], v[100:101], v[100:101], s[22:23] neg_lo:[1,0,0] neg_hi:[1,0,0]
	v_pk_fma_f32 v[102:103], v[102:103], v[102:103], s[22:23] neg_lo:[1,0,0] neg_hi:[1,0,0]
	v_exp_f32_e32 v96, v96
	v_exp_f32_e32 v97, v97
	v_exp_f32_e32 v98, v98
	v_exp_f32_e32 v99, v99
	v_exp_f32_e32 v100, v100
	v_exp_f32_e32 v101, v101
	v_exp_f32_e32 v102, v102
	v_exp_f32_e32 v103, v103
	v_pk_add_f32 v[66:67], v[66:67], v[104:105]
	v_pk_fma_f32 v[70:71], v[104:105], v[26:27], v[70:71]
	v_pk_add_f32 v[72:73], v[72:73], v[104:105]
	v_pk_fma_f32 v[76:77], v[104:105], v[20:21], v[76:77]
	v_pk_add_f32 v[66:67], v[66:67], v[106:107]
	v_pk_fma_f32 v[70:71], v[106:107], v[28:29], v[70:71]
	v_pk_add_f32 v[74:75], v[74:75], v[106:107]
	v_pk_fma_f32 v[78:79], v[106:107], v[20:21], v[78:79]
	v_pk_add_f32 v[66:67], v[66:67], v[108:109]
	v_pk_fma_f32 v[70:71], v[108:109], v[30:31], v[70:71]
	v_pk_add_f32 v[74:75], v[74:75], v[110:111]
	v_pk_fma_f32 v[78:79], v[110:111], v[22:23], v[78:79]
	v_pk_add_f32 v[104:105], v[30:31], v[28:29] neg_lo:[0,1] neg_hi:[0,1]
	v_pk_fma_f32 v[104:105], v[104:105], v[104:105], s[22:23] neg_lo:[1,0,0] neg_hi:[1,0,0]
	s_nop 0
	v_exp_f32_e32 v104, v104
	v_exp_f32_e64 v105, v105
	v_pk_add_f32 v[64:65], v[64:65], v[96:97]
	v_pk_fma_f32 v[68:69], v[96:97], v[26:27], v[68:69] op_sel:[0,1,0] op_sel_hi:[1,0,1]
	v_pk_add_f32 v[72:73], v[72:73], v[96:97] op_sel:[0,1] op_sel_hi:[1,0]
	v_pk_fma_f32 v[76:77], v[96:97], v[18:19], v[76:77] op_sel:[1,1,0] op_sel_hi:[0,0,1]
	v_pk_add_f32 v[66:67], v[66:67], v[98:99]
	v_pk_fma_f32 v[70:71], v[98:99], v[28:29], v[70:71] op_sel:[0,1,0] op_sel_hi:[1,0,1]
	v_pk_add_f32 v[74:75], v[74:75], v[98:99] op_sel:[0,1] op_sel_hi:[1,0]
	v_pk_fma_f32 v[78:79], v[98:99], v[20:21], v[78:79] op_sel:[1,1,0] op_sel_hi:[0,0,1]
	v_pk_add_f32 v[72:73], v[72:73], v[100:101]
	v_pk_fma_f32 v[76:77], v[100:101], v[24:25], v[76:77]
	v_pk_add_f32 v[74:75], v[74:75], v[102:103]
	v_pk_add_f32 v[72:73], v[72:73], v[102:103]
	v_pk_fma_f32 v[76:77], v[102:103], v[28:29], v[76:77]
	v_pk_fma_f32 v[78:79], v[102:103], v[26:27], v[78:79]
	s_nop 0
	v_sub_f32_e32 v96, v26, v9
	v_sub_f32_e32 v98, v28, v11
	v_sub_f32_e32 v100, v27, v12
	v_sub_f32_e32 v102, v29, v14
	v_sub_f32_e32 v97, v26, v17
	v_sub_f32_e32 v99, v25, v18
	v_sub_f32_e32 v101, v28, v19
	v_sub_f32_e64 v103, v27, v20
	v_fma_f32 v96, -v96, v96, s26
	v_fma_f32 v98, -v98, v98, s26
	v_fma_f32 v100, -v100, v100, s26
	v_fma_f32 v102, -v102, v102, s26
	v_fma_f32 v97, -v97, v97, s24
	v_fma_f32 v99, -v99, v99, s24
	v_fma_f32 v101, -v101, v101, s24
	v_fma_f32 v103, -v103, v103, s24
	v_exp_f32_e32 v96, v96
	v_exp_f32_e32 v98, v98
	v_exp_f32_e32 v100, v100
	v_exp_f32_e32 v102, v102
	v_exp_f32_e32 v97, v97
	v_exp_f32_e32 v99, v99
	v_exp_f32_e32 v101, v101
	v_exp_f32_e32 v103, v103
	v_pk_add_f32 v[74:75], v[74:75], v[104:105]
	v_pk_fma_f32 v[78:79], v[104:105], v[30:31], v[78:79]
	v_sub_f32_e32 v108, v30, v21
	v_sub_f32_e32 v110, v29, v22
	v_sub_f32_e32 v105, v26, v25
	v_sub_f32_e32 v104, v27, v26
	v_sub_f32_e32 v107, v28, v27
	v_sub_f32_e32 v106, v29, v28
	v_sub_f32_e64 v109, v30, v29
	v_fma_f32 v108, -v108, v108, s24
	v_fma_f32 v110, -v110, v110, s24
	v_fma_f32 v105, -v105, v105, s20
	v_fma_f32 v104, -v104, v104, s20
	v_fma_f32 v107, -v107, v107, s20
	v_fma_f32 v106, -v106, v106, s20
	v_fma_f32 v109, -v109, v109, s20
	v_exp_f32_e32 v108, v108
	v_exp_f32_e32 v110, v110
	v_exp_f32_e32 v105, v105
	v_exp_f32_e32 v104, v104
	v_exp_f32_e32 v107, v107
	v_exp_f32_e32 v106, v106
	v_exp_f32_e32 v109, v109
	v_add_f32_e32 v72, v72, v96
	v_fmac_f32_e32 v76, v96, v9
	v_add_f32_e32 v74, v74, v98
	v_fmac_f32_e32 v78, v98, v11
	v_add_f32_e32 v73, v73, v100
	v_fmac_f32_e32 v77, v100, v12
	v_add_f32_e32 v75, v75, v102
	v_fmac_f32_e32 v79, v102, v14
	v_add_f32_e32 v72, v72, v97
	v_fmac_f32_e32 v76, v97, v17
	v_add_f32_e32 v64, v64, v99
	v_fmac_f32_e32 v68, v99, v25
	v_add_f32_e32 v65, v65, v101
	v_fmac_f32_e32 v69, v101, v28
	v_add_f32_e32 v74, v74, v101
	v_fmac_f32_e32 v78, v101, v19
	v_add_f32_e32 v66, v66, v103
	v_fmac_f32_e32 v70, v103, v27
	v_add_f32_e32 v73, v73, v103
	v_fmac_f32_e32 v77, v103, v20
	v_add_f32_e32 v67, v67, v108
	v_fmac_f32_e32 v71, v108, v30
	v_add_f32_e32 v75, v75, v110
	v_fmac_f32_e32 v79, v110, v22
	v_add_f32_e32 v72, v72, v105
	v_fmac_f32_e32 v76, v105, v25
	v_add_f32_e32 v73, v73, v107
	v_fmac_f32_e32 v77, v107, v28
	v_add_f32_e32 v74, v74, v107
	v_fmac_f32_e32 v78, v107, v27
	v_add_f32_e32 v75, v75, v109
	v_fmac_f32_e64 v79, v109, v30
	v_pk_add_f32 v[72:73], v[72:73], v[104:105] op_sel_hi:[1,0]
	v_pk_fma_f32 v[76:77], v[104:105], v[26:27], v[76:77] op_sel:[0,1,0] op_sel_hi:[0,0,1]
	v_pk_add_f32 v[74:75], v[74:75], v[106:107] op_sel_hi:[1,0]
	v_pk_fma_f32 v[78:79], v[106:107], v[28:29], v[78:79] op_sel:[0,1,0] op_sel_hi:[0,0,1]
	s_waitcnt vmcnt(9)
	s_nop 0
	v_mov_b32_dpp v32, v36 row_shr:1 row_mask:0xf bank_mask:0xf
	v_mov_b32_dpp v33, v37 row_shr:1 row_mask:0xf bank_mask:0xf
	v_mov_b32_dpp v38, v34 row_shl:1 row_mask:0xf bank_mask:0xf
	v_mov_b32_dpp v39, v35 row_shl:1 row_mask:0xf bank_mask:0xf
	v_pk_mul_f32 v[34:35], v[34:35], s[32:33]
	v_pk_mul_f32 v[36:37], v[36:37], s[32:33]
	v_cndmask_b32_e64 v33, v33, v32, vcc
	v_cndmask_b32_e64 v38, v38, v39, s[16:17]
	v_pk_mul_f32 v[84:85], v[34:35], s[30:31]
	v_pk_mul_f32 v[86:87], v[36:37], s[30:31]
	v_pk_mul_f32 v[32:33], v[32:33], s[32:33]
	v_pk_mul_f32 v[38:39], v[38:39], s[32:33]
	v_pk_add_f32 v[96:97], v[34:35], v[16:17] neg_lo:[0,1] neg_hi:[0,1]
	v_pk_add_f32 v[98:99], v[32:33], v[18:19] neg_lo:[0,1] neg_hi:[0,1]
	v_pk_add_f32 v[100:101], v[34:35], v[18:19] neg_lo:[0,1] neg_hi:[0,1]
	v_pk_add_f32 v[102:103], v[36:37], v[18:19] neg_lo:[0,1] neg_hi:[0,1]
	v_pk_fma_f32 v[96:97], v[96:97], v[96:97], s[28:29] neg_lo:[1,0,0] neg_hi:[1,0,0]
	v_pk_fma_f32 v[98:99], v[98:99], v[98:99], s[28:29] neg_lo:[1,0,0] neg_hi:[1,0,0]
	v_pk_fma_f32 v[100:101], v[100:101], v[100:101], s[22:23] neg_lo:[1,0,0] neg_hi:[1,0,0]
	v_pk_fma_f32 v[102:103], v[102:103], v[102:103], s[28:29] neg_lo:[1,0,0] neg_hi:[1,0,0]
	v_exp_f32_e32 v96, v96
	v_exp_f32_e32 v97, v97
	v_exp_f32_e32 v98, v98
	v_exp_f32_e32 v99, v99
	v_exp_f32_e32 v100, v100
	v_exp_f32_e32 v101, v101
	v_exp_f32_e32 v102, v102
	v_exp_f32_e32 v103, v103
	v_pk_add_f32 v[104:105], v[34:35], v[20:21] neg_lo:[0,1] neg_hi:[0,1]
	v_pk_add_f32 v[106:107], v[36:37], v[20:21] neg_lo:[0,1] neg_hi:[0,1]
	v_pk_add_f32 v[108:109], v[38:39], v[20:21] neg_lo:[0,1] neg_hi:[0,1]
	v_pk_add_f32 v[110:111], v[36:37], v[22:23] neg_lo:[0,1] neg_hi:[0,1]
	v_pk_fma_f32 v[104:105], v[104:105], v[104:105], s[28:29] neg_lo:[1,0,0] neg_hi:[1,0,0]
	v_pk_fma_f32 v[106:107], v[106:107], v[106:107], s[22:23] neg_lo:[1,0,0] neg_hi:[1,0,0]
	v_pk_fma_f32 v[108:109], v[108:109], v[108:109], s[28:29] neg_lo:[1,0,0] neg_hi:[1,0,0]
	v_pk_fma_f32 v[110:111], v[110:111], v[110:111], s[28:29] neg_lo:[1,0,0] neg_hi:[1,0,0]
	v_exp_f32_e32 v104, v104
	v_exp_f32_e32 v105, v105
	v_exp_f32_e32 v106, v106
	v_exp_f32_e32 v107, v107
	v_exp_f32_e32 v108, v108
	v_exp_f32_e32 v109, v109
	v_exp_f32_e32 v110, v110
	v_exp_f32_e32 v111, v111
	v_pk_add_f32 v[80:81], s[30:31], v[96:97]
	v_pk_fma_f32 v[84:85], v[96:97], v[16:17], v[84:85]
	v_pk_add_f32 v[64:65], v[64:65], v[98:99]
	v_pk_fma_f32 v[68:69], v[98:99], v[32:33], v[68:69]
	v_pk_add_f32 v[80:81], v[80:81], v[100:101]
	v_pk_add_f32 v[64:65], v[64:65], v[100:101]
	v_pk_fma_f32 v[68:69], v[100:101], v[34:35], v[68:69]
	v_pk_fma_f32 v[84:85], v[100:101], v[18:19], v[84:85]
	v_pk_add_f32 v[64:65], v[64:65], v[102:103]
	v_pk_fma_f32 v[68:69], v[102:103], v[36:37], v[68:69]
	v_pk_add_f32 v[82:83], s[30:31], v[102:103]
	v_pk_fma_f32 v[86:87], v[102:103], v[18:19], v[86:87]
	v_pk_add_f32 v[96:97], v[34:35], v[18:19] op_sel:[1,0] op_sel_hi:[0,1] neg_lo:[0,1] neg_hi:[0,1]
	v_pk_add_f32 v[98:99], v[36:37], v[20:21] op_sel:[1,0] op_sel_hi:[0,1] neg_lo:[0,1] neg_hi:[0,1]
	v_pk_add_f32 v[100:101], v[34:35], v[24:25] neg_lo:[0,1] neg_hi:[0,1]
	v_pk_add_f32 v[102:103], v[32:33], v[26:27] neg_lo:[0,1] neg_hi:[0,1]
	v_pk_fma_f32 v[96:97], v[96:97], v[96:97], s[26:27] neg_lo:[1,0,0] neg_hi:[1,0,0]
	v_pk_fma_f32 v[98:99], v[98:99], v[98:99], s[26:27] neg_lo:[1,0,0] neg_hi:[1,0,0]
	v_pk_fma_f32 v[100:101], v[100:101], v[100:101], s[26:27] neg_lo:[1,0,0] neg_hi:[1,0,0]
	v_pk_fma_f32 v[102:103], v[102:103], v[102:103], s[26:27] neg_lo:[1,0,0] neg_hi:[1,0,0]
	v_exp_f32_e32 v96, v96
	v_exp_f32_e32 v97, v97
	v_exp_f32_e32 v98, v98
	v_exp_f32_e32 v99, v99
	v_exp_f32_e32 v100, v100
	v_exp_f32_e32 v101, v101
	v_exp_f32_e32 v102, v102
	v_exp_f32_e32 v103, v103
	v_pk_add_f32 v[66:67], v[66:67], v[104:105]
	v_pk_fma_f32 v[70:71], v[104:105], v[34:35], v[70:71]
	v_pk_add_f32 v[80:81], v[80:81], v[104:105]
	v_pk_fma_f32 v[84:85], v[104:105], v[20:21], v[84:85]
	v_pk_add_f32 v[66:67], v[66:67], v[106:107]
	v_pk_fma_f32 v[70:71], v[106:107], v[36:37], v[70:71]
	v_pk_add_f32 v[82:83], v[82:83], v[106:107]
	v_pk_fma_f32 v[86:87], v[106:107], v[20:21], v[86:87]
	v_pk_add_f32 v[66:67], v[66:67], v[108:109]
	v_pk_fma_f32 v[70:71], v[108:109], v[38:39], v[70:71]
	v_pk_add_f32 v[82:83], v[82:83], v[110:111]
	v_pk_fma_f32 v[86:87], v[110:111], v[22:23], v[86:87]
	v_pk_add_f32 v[104:105], v[34:35], v[26:27] neg_lo:[0,1] neg_hi:[0,1]
	v_pk_add_f32 v[106:107], v[36:37], v[26:27] neg_lo:[0,1] neg_hi:[0,1]
	v_pk_add_f32 v[108:109], v[34:35], v[28:29] neg_lo:[0,1] neg_hi:[0,1]
	v_pk_add_f32 v[110:111], v[36:37], v[28:29] neg_lo:[0,1] neg_hi:[0,1]
	v_pk_fma_f32 v[104:105], v[104:105], v[104:105], s[20:21] neg_lo:[1,0,0] neg_hi:[1,0,0]
	v_pk_fma_f32 v[106:107], v[106:107], v[106:107], s[26:27] neg_lo:[1,0,0] neg_hi:[1,0,0]
	v_pk_fma_f32 v[108:109], v[108:109], v[108:109], s[26:27] neg_lo:[1,0,0] neg_hi:[1,0,0]
	v_pk_fma_f32 v[110:111], v[110:111], v[110:111], s[20:21] neg_lo:[1,0,0] neg_hi:[1,0,0]
	v_exp_f32_e32 v104, v104
	v_exp_f32_e32 v105, v105
	v_exp_f32_e32 v106, v106
	v_exp_f32_e32 v107, v107
	v_exp_f32_e32 v108, v108
	v_exp_f32_e32 v109, v109
	v_exp_f32_e32 v110, v110
	v_exp_f32_e32 v111, v111
	v_pk_add_f32 v[64:65], v[64:65], v[96:97]
	v_pk_fma_f32 v[68:69], v[96:97], v[34:35], v[68:69] op_sel:[0,1,0] op_sel_hi:[1,0,1]
	v_pk_add_f32 v[80:81], v[80:81], v[96:97] op_sel:[0,1] op_sel_hi:[1,0]
	v_pk_fma_f32 v[84:85], v[96:97], v[18:19], v[84:85] op_sel:[1,1,0] op_sel_hi:[0,0,1]
	v_pk_add_f32 v[66:67], v[66:67], v[98:99]
	v_pk_fma_f32 v[70:71], v[98:99], v[36:37], v[70:71] op_sel:[0,1,0] op_sel_hi:[1,0,1]
	v_pk_add_f32 v[82:83], v[82:83], v[98:99] op_sel:[0,1] op_sel_hi:[1,0]
	v_pk_fma_f32 v[86:87], v[98:99], v[20:21], v[86:87] op_sel:[1,1,0] op_sel_hi:[0,0,1]
	v_pk_add_f32 v[80:81], v[80:81], v[100:101]
	v_pk_fma_f32 v[84:85], v[100:101], v[24:25], v[84:85]
	v_pk_add_f32 v[72:73], v[72:73], v[102:103]
	v_pk_fma_f32 v[76:77], v[102:103], v[32:33], v[76:77]
	v_pk_add_f32 v[96:97], v[38:39], v[28:29] neg_lo:[0,1] neg_hi:[0,1]
	v_pk_add_f32 v[98:99], v[36:37], v[30:31] neg_lo:[0,1] neg_hi:[0,1]
	v_pk_add_f32 v[100:101], v[34:35], v[26:27] op_sel:[1,0] op_sel_hi:[0,1] neg_lo:[0,1] neg_hi:[0,1]
	v_pk_add_f32 v[102:103], v[36:37], v[28:29] op_sel:[1,0] op_sel_hi:[0,1] neg_lo:[0,1] neg_hi:[0,1]
	v_pk_fma_f32 v[96:97], v[96:97], v[96:97], s[26:27] neg_lo:[1,0,0] neg_hi:[1,0,0]
	v_pk_fma_f32 v[98:99], v[98:99], v[98:99], s[26:27] neg_lo:[1,0,0] neg_hi:[1,0,0]
	v_pk_fma_f32 v[100:101], v[100:101], v[100:101], s[24:25] neg_lo:[1,0,0] neg_hi:[1,0,0]
	v_pk_fma_f32 v[102:103], v[102:103], v[102:103], s[24:25] neg_lo:[1,0,0] neg_hi:[1,0,0]
	v_exp_f32_e32 v96, v96
	v_exp_f32_e32 v97, v97
	v_exp_f32_e32 v98, v98
	v_exp_f32_e32 v99, v99
	v_exp_f32_e32 v100, v100
	v_exp_f32_e32 v101, v101
	v_exp_f32_e32 v102, v102
	v_exp_f32_e32 v103, v103
	v_pk_add_f32 v[72:73], v[72:73], v[104:105]
	v_pk_fma_f32 v[76:77], v[104:105], v[34:35], v[76:77]
	v_pk_add_f32 v[80:81], v[80:81], v[104:105]
	v_pk_fma_f32 v[84:85], v[104:105], v[26:27], v[84:85]
	v_pk_add_f32 v[72:73], v[72:73], v[106:107]
	v_pk_fma_f32 v[76:77], v[106:107], v[36:37], v[76:77]
	v_pk_add_f32 v[82:83], v[82:83], v[106:107]
	v_pk_fma_f32 v[86:87], v[106:107], v[26:27], v[86:87]
	v_pk_add_f32 v[74:75], v[74:75], v[108:109]
	v_pk_fma_f32 v[78:79], v[108:109], v[34:35], v[78:79]
	v_pk_add_f32 v[80:81], v[80:81], v[108:109]
	v_pk_fma_f32 v[84:85], v[108:109], v[28:29], v[84:85]
	v_pk_add_f32 v[74:75], v[74:75], v[110:111]
	v_pk_fma_f32 v[78:79], v[110:111], v[36:37], v[78:79]
	v_pk_add_f32 v[82:83], v[82:83], v[110:111]
	v_pk_fma_f32 v[86:87], v[110:111], v[28:29], v[86:87]
	v_pk_add_f32 v[104:105], v[34:35], v[32:33] neg_lo:[0,1] neg_hi:[0,1]
	v_pk_add_f32 v[106:107], v[36:37], v[34:35] neg_lo:[0,1] neg_hi:[0,1]
	v_pk_add_f32 v[108:109], v[38:39], v[36:37] neg_lo:[0,1] neg_hi:[0,1]
	v_pk_fma_f32 v[104:105], v[104:105], v[104:105], s[22:23] neg_lo:[1,0,0] neg_hi:[1,0,0]
	v_pk_fma_f32 v[106:107], v[106:107], v[106:107], s[22:23] neg_lo:[1,0,0] neg_hi:[1,0,0]
	v_pk_fma_f32 v[108:109], v[108:109], v[108:109], s[22:23] neg_lo:[1,0,0] neg_hi:[1,0,0]
	v_exp_f32_e32 v104, v104
	v_exp_f32_e32 v105, v105
	v_exp_f32_e32 v106, v106
	v_exp_f32_e32 v107, v107
	v_exp_f32_e32 v108, v108
	v_exp_f32_e32 v109, v109
	v_pk_add_f32 v[74:75], v[74:75], v[96:97]
	v_pk_fma_f32 v[78:79], v[96:97], v[38:39], v[78:79]
	v_pk_add_f32 v[82:83], v[82:83], v[98:99]
	v_pk_fma_f32 v[86:87], v[98:99], v[30:31], v[86:87]
	v_pk_add_f32 v[72:73], v[72:73], v[100:101]
	v_pk_fma_f32 v[76:77], v[100:101], v[34:35], v[76:77] op_sel:[0,1,0] op_sel_hi:[1,0,1]
	v_pk_add_f32 v[80:81], v[80:81], v[100:101] op_sel:[0,1] op_sel_hi:[1,0]
	v_pk_fma_f32 v[84:85], v[100:101], v[26:27], v[84:85] op_sel:[1,1,0] op_sel_hi:[0,0,1]
	v_pk_add_f32 v[74:75], v[74:75], v[102:103]
	v_pk_fma_f32 v[78:79], v[102:103], v[36:37], v[78:79] op_sel:[0,1,0] op_sel_hi:[1,0,1]
	v_pk_add_f32 v[82:83], v[82:83], v[102:103] op_sel:[0,1] op_sel_hi:[1,0]
	v_pk_fma_f32 v[86:87], v[102:103], v[28:29], v[86:87] op_sel:[1,1,0] op_sel_hi:[0,0,1]
	v_sub_f32_e32 v96, v34, v17
	v_sub_f32_e32 v98, v33, v18
	v_sub_f32_e32 v100, v36, v19
	v_sub_f32_e32 v102, v35, v20
	v_sub_f32_e32 v97, v38, v21
	v_sub_f32_e32 v99, v37, v22
	v_sub_f32_e32 v101, v34, v25
	v_sub_f32_e32 v103, v33, v26
	v_fma_f32 v96, -v96, v96, s26
	v_fma_f32 v98, -v98, v98, s26
	v_fma_f32 v100, -v100, v100, s26
	v_fma_f32 v102, -v102, v102, s26
	v_fma_f32 v97, -v97, v97, s26
	v_fma_f32 v99, -v99, v99, s26
	v_fma_f32 v101, -v101, v101, s24
	v_fma_f32 v103, -v103, v103, s24
	v_exp_f32_e32 v96, v96
	v_exp_f32_e32 v98, v98
	v_exp_f32_e32 v100, v100
	v_exp_f32_e32 v102, v102
	v_exp_f32_e32 v97, v97
	v_exp_f32_e32 v99, v99
	v_exp_f32_e32 v101, v101
	v_exp_f32_e32 v103, v103
	v_pk_add_f32 v[80:81], v[80:81], v[104:105]
	v_pk_fma_f32 v[84:85], v[104:105], v[32:33], v[84:85]
	v_pk_add_f32 v[82:83], v[82:83], v[106:107]
	v_pk_add_f32 v[80:81], v[80:81], v[106:107]
	v_pk_fma_f32 v[84:85], v[106:107], v[36:37], v[84:85]
	v_pk_fma_f32 v[86:87], v[106:107], v[34:35], v[86:87]
	v_pk_add_f32 v[82:83], v[82:83], v[108:109]
	v_pk_fma_f32 v[86:87], v[108:109], v[38:39], v[86:87]
	v_sub_f32_e32 v108, v36, v27
	v_sub_f32_e32 v110, v35, v28
	v_sub_f32_e32 v105, v38, v29
	v_sub_f32_e32 v107, v37, v30
	v_sub_f32_e32 v109, v34, v33
	v_sub_f32_e32 v104, v35, v34
	v_sub_f32_e32 v111, v36, v35
	v_sub_f32_e32 v106, v37, v36
	v_fma_f32 v108, -v108, v108, s24
	v_fma_f32 v110, -v110, v110, s24
	v_fma_f32 v105, -v105, v105, s24
	v_fma_f32 v107, -v107, v107, s24
	v_fma_f32 v109, -v109, v109, s20
	v_fma_f32 v104, -v104, v104, s20
	v_fma_f32 v111, -v111, v111, s20
	v_fma_f32 v106, -v106, v106, s20
	v_exp_f32_e32 v108, v108
	v_exp_f32_e32 v110, v110
	v_exp_f32_e32 v105, v105
	v_exp_f32_e32 v107, v107
	v_exp_f32_e32 v109, v109
	v_exp_f32_e32 v104, v104
	v_exp_f32_e32 v111, v111
	v_exp_f32_e32 v106, v106
	v_add_f32_e32 v80, v80, v96
	v_fmac_f32_e32 v84, v96, v17
	v_add_f32_e32 v64, v64, v98
	v_fmac_f32_e32 v68, v98, v33
	v_add_f32_e32 v65, v65, v100
	v_fmac_f32_e32 v69, v100, v36
	v_add_f32_e32 v82, v82, v100
	v_fmac_f32_e32 v86, v100, v19
	v_add_f32_e32 v66, v66, v102
	v_fmac_f32_e32 v70, v102, v35
	v_add_f32_e32 v81, v81, v102
	v_fmac_f32_e32 v85, v102, v20
	v_add_f32_e32 v67, v67, v97
	v_fmac_f32_e32 v71, v97, v38
	v_add_f32_e32 v83, v83, v99
	v_fmac_f32_e32 v87, v99, v22
	v_add_f32_e32 v80, v80, v101
	v_fmac_f32_e32 v84, v101, v25
	v_add_f32_e32 v72, v72, v103
	v_fmac_f32_e32 v76, v103, v33
	v_sub_f32_e64 v96, v38, v37
	v_fma_f32 v96, -v96, v96, s20
	s_nop 0
	v_exp_f32_e32 v96, v96
	v_add_f32_e32 v73, v73, v108
	v_fmac_f32_e32 v77, v108, v36
	v_add_f32_e32 v82, v82, v108
	v_fmac_f32_e32 v86, v108, v27
	v_add_f32_e32 v74, v74, v110
	v_fmac_f32_e32 v78, v110, v35
	v_add_f32_e32 v81, v81, v110
	v_fmac_f32_e32 v85, v110, v28
	v_add_f32_e32 v75, v75, v105
	v_fmac_f32_e32 v79, v105, v38
	v_add_f32_e32 v83, v83, v107
	v_fmac_f32_e32 v87, v107, v30
	v_add_f32_e32 v80, v80, v109
	v_fmac_f32_e32 v84, v109, v33
	v_add_f32_e32 v81, v81, v111
	v_fmac_f32_e32 v85, v111, v36
	v_add_f32_e32 v82, v82, v111
	v_fmac_f32_e32 v86, v111, v35
	v_pk_add_f32 v[80:81], v[80:81], v[104:105] op_sel_hi:[1,0]
	v_pk_fma_f32 v[84:85], v[104:105], v[34:35], v[84:85] op_sel:[0,1,0] op_sel_hi:[0,0,1]
	v_pk_add_f32 v[82:83], v[82:83], v[106:107] op_sel_hi:[1,0]
	v_pk_fma_f32 v[86:87], v[106:107], v[36:37], v[86:87] op_sel:[0,1,0] op_sel_hi:[0,0,1]
	s_nop 0
	v_add_f32_e32 v83, v83, v96
	v_fmac_f32_e32 v87, v96, v38
	v_rcp_f32_e32 v96, v64
	v_rcp_f32_e32 v97, v65
	v_rcp_f32_e32 v98, v66
	v_rcp_f32_e64 v99, v67
	v_pk_mul_f32 v[68:69], v[68:69], s[34:35]
	v_pk_mul_f32 v[70:71], v[70:71], s[34:35]
	v_pk_mul_f32 v[68:69], v[68:69], v[96:97]
	v_pk_mul_f32 v[70:71], v[70:71], v[98:99]
	buffer_store_dwordx4 v[68:71], v114, s[12:15], 0 offen sc1
	s_waitcnt vmcnt(7)
	s_nop 0
	v_mov_b32_dpp v40, v44 row_shr:1 row_mask:0xf bank_mask:0xf
	v_mov_b32_dpp v41, v45 row_shr:1 row_mask:0xf bank_mask:0xf
	v_mov_b32_dpp v46, v42 row_shl:1 row_mask:0xf bank_mask:0xf
	v_mov_b32_dpp v47, v43 row_shl:1 row_mask:0xf bank_mask:0xf
	v_pk_mul_f32 v[42:43], v[42:43], s[32:33]
	v_pk_mul_f32 v[44:45], v[44:45], s[32:33]
	v_cndmask_b32_e64 v41, v41, v40, vcc
	v_cndmask_b32_e64 v46, v46, v47, s[16:17]
	v_pk_mul_f32 v[92:93], v[42:43], s[30:31]
	v_pk_mul_f32 v[94:95], v[44:45], s[30:31]
	v_pk_mul_f32 v[40:41], v[40:41], s[32:33]
	v_pk_mul_f32 v[46:47], v[46:47], s[32:33]
	v_pk_add_f32 v[96:97], v[42:43], v[24:25] neg_lo:[0,1] neg_hi:[0,1]
	v_pk_add_f32 v[98:99], v[40:41], v[26:27] neg_lo:[0,1] neg_hi:[0,1]
	v_pk_add_f32 v[100:101], v[42:43], v[26:27] neg_lo:[0,1] neg_hi:[0,1]
	v_pk_add_f32 v[102:103], v[44:45], v[26:27] neg_lo:[0,1] neg_hi:[0,1]
	v_pk_fma_f32 v[96:97], v[96:97], v[96:97], s[28:29] neg_lo:[1,0,0] neg_hi:[1,0,0]
	v_pk_fma_f32 v[98:99], v[98:99], v[98:99], s[28:29] neg_lo:[1,0,0] neg_hi:[1,0,0]
	v_pk_fma_f32 v[100:101], v[100:101], v[100:101], s[22:23] neg_lo:[1,0,0] neg_hi:[1,0,0]
	v_pk_fma_f32 v[102:103], v[102:103], v[102:103], s[28:29] neg_lo:[1,0,0] neg_hi:[1,0,0]
	v_exp_f32_e32 v96, v96
	v_exp_f32_e32 v97, v97
	v_exp_f32_e32 v98, v98
	v_exp_f32_e32 v99, v99
	v_exp_f32_e32 v100, v100
	v_exp_f32_e32 v101, v101
	v_exp_f32_e32 v102, v102
	v_exp_f32_e32 v103, v103
	v_pk_add_f32 v[104:105], v[42:43], v[28:29] neg_lo:[0,1] neg_hi:[0,1]
	v_pk_add_f32 v[106:107], v[44:45], v[28:29] neg_lo:[0,1] neg_hi:[0,1]
	v_pk_add_f32 v[108:109], v[46:47], v[28:29] neg_lo:[0,1] neg_hi:[0,1]
	v_pk_add_f32 v[110:111], v[44:45], v[30:31] neg_lo:[0,1] neg_hi:[0,1]
	v_pk_fma_f32 v[104:105], v[104:105], v[104:105], s[28:29] neg_lo:[1,0,0] neg_hi:[1,0,0]
	v_pk_fma_f32 v[106:107], v[106:107], v[106:107], s[22:23] neg_lo:[1,0,0] neg_hi:[1,0,0]
	v_pk_fma_f32 v[108:109], v[108:109], v[108:109], s[28:29] neg_lo:[1,0,0] neg_hi:[1,0,0]
	v_pk_fma_f32 v[110:111], v[110:111], v[110:111], s[28:29] neg_lo:[1,0,0] neg_hi:[1,0,0]
	v_exp_f32_e32 v104, v104
	v_exp_f32_e32 v105, v105
	v_exp_f32_e32 v106, v106
	v_exp_f32_e32 v107, v107
	v_exp_f32_e32 v108, v108
	v_exp_f32_e32 v109, v109
	v_exp_f32_e32 v110, v110
	v_exp_f32_e32 v111, v111
	v_pk_add_f32 v[88:89], s[30:31], v[96:97]
	v_pk_fma_f32 v[92:93], v[96:97], v[24:25], v[92:93]
	v_pk_add_f32 v[72:73], v[72:73], v[98:99]
	v_pk_fma_f32 v[76:77], v[98:99], v[40:41], v[76:77]
	v_pk_add_f32 v[88:89], v[88:89], v[100:101]
	v_pk_add_f32 v[72:73], v[72:73], v[100:101]
	v_pk_fma_f32 v[76:77], v[100:101], v[42:43], v[76:77]
	v_pk_fma_f32 v[92:93], v[100:101], v[26:27], v[92:93]
	v_pk_add_f32 v[72:73], v[72:73], v[102:103]
	v_pk_fma_f32 v[76:77], v[102:103], v[44:45], v[76:77]
	v_pk_add_f32 v[90:91], s[30:31], v[102:103]
	v_pk_fma_f32 v[94:95], v[102:103], v[26:27], v[94:95]
	v_pk_add_f32 v[96:97], v[42:43], v[26:27] op_sel:[1,0] op_sel_hi:[0,1] neg_lo:[0,1] neg_hi:[0,1]
	v_pk_add_f32 v[98:99], v[44:45], v[28:29] op_sel:[1,0] op_sel_hi:[0,1] neg_lo:[0,1] neg_hi:[0,1]
	v_pk_add_f32 v[100:101], v[42:43], v[32:33] neg_lo:[0,1] neg_hi:[0,1]
	v_pk_add_f32 v[102:103], v[40:41], v[34:35] neg_lo:[0,1] neg_hi:[0,1]
	v_pk_fma_f32 v[96:97], v[96:97], v[96:97], s[26:27] neg_lo:[1,0,0] neg_hi:[1,0,0]
	v_pk_fma_f32 v[98:99], v[98:99], v[98:99], s[26:27] neg_lo:[1,0,0] neg_hi:[1,0,0]
	v_pk_fma_f32 v[100:101], v[100:101], v[100:101], s[26:27] neg_lo:[1,0,0] neg_hi:[1,0,0]
	v_pk_fma_f32 v[102:103], v[102:103], v[102:103], s[26:27] neg_lo:[1,0,0] neg_hi:[1,0,0]
	v_exp_f32_e32 v96, v96
	v_exp_f32_e32 v97, v97
	v_exp_f32_e32 v98, v98
	v_exp_f32_e32 v99, v99
	v_exp_f32_e32 v100, v100
	v_exp_f32_e32 v101, v101
	v_exp_f32_e32 v102, v102
	v_exp_f32_e32 v103, v103
	v_pk_add_f32 v[74:75], v[74:75], v[104:105]
	v_pk_fma_f32 v[78:79], v[104:105], v[42:43], v[78:79]
	v_pk_add_f32 v[88:89], v[88:89], v[104:105]
	v_pk_fma_f32 v[92:93], v[104:105], v[28:29], v[92:93]
	v_pk_add_f32 v[74:75], v[74:75], v[106:107]
	v_pk_fma_f32 v[78:79], v[106:107], v[44:45], v[78:79]
	v_pk_add_f32 v[90:91], v[90:91], v[106:107]
	v_pk_fma_f32 v[94:95], v[106:107], v[28:29], v[94:95]
	v_pk_add_f32 v[74:75], v[74:75], v[108:109]
	v_pk_fma_f32 v[78:79], v[108:109], v[46:47], v[78:79]
	v_pk_add_f32 v[90:91], v[90:91], v[110:111]
	v_pk_fma_f32 v[94:95], v[110:111], v[30:31], v[94:95]
	v_pk_add_f32 v[104:105], v[42:43], v[34:35] neg_lo:[0,1] neg_hi:[0,1]
	v_pk_add_f32 v[106:107], v[44:45], v[34:35] neg_lo:[0,1] neg_hi:[0,1]
	v_pk_add_f32 v[108:109], v[42:43], v[36:37] neg_lo:[0,1] neg_hi:[0,1]
	v_pk_add_f32 v[110:111], v[44:45], v[36:37] neg_lo:[0,1] neg_hi:[0,1]
	v_pk_fma_f32 v[104:105], v[104:105], v[104:105], s[20:21] neg_lo:[1,0,0] neg_hi:[1,0,0]
	v_pk_fma_f32 v[106:107], v[106:107], v[106:107], s[26:27] neg_lo:[1,0,0] neg_hi:[1,0,0]
	v_pk_fma_f32 v[108:109], v[108:109], v[108:109], s[26:27] neg_lo:[1,0,0] neg_hi:[1,0,0]
	v_pk_fma_f32 v[110:111], v[110:111], v[110:111], s[20:21] neg_lo:[1,0,0] neg_hi:[1,0,0]
	v_exp_f32_e32 v104, v104
	v_exp_f32_e32 v105, v105
	v_exp_f32_e32 v106, v106
	v_exp_f32_e32 v107, v107
	v_exp_f32_e32 v108, v108
	v_exp_f32_e32 v109, v109
	v_exp_f32_e32 v110, v110
	v_exp_f32_e32 v111, v111
	v_pk_add_f32 v[72:73], v[72:73], v[96:97]
	v_pk_fma_f32 v[76:77], v[96:97], v[42:43], v[76:77] op_sel:[0,1,0] op_sel_hi:[1,0,1]
	v_pk_add_f32 v[88:89], v[88:89], v[96:97] op_sel:[0,1] op_sel_hi:[1,0]
	v_pk_fma_f32 v[92:93], v[96:97], v[26:27], v[92:93] op_sel:[1,1,0] op_sel_hi:[0,0,1]
	v_pk_add_f32 v[74:75], v[74:75], v[98:99]
	v_pk_fma_f32 v[78:79], v[98:99], v[44:45], v[78:79] op_sel:[0,1,0] op_sel_hi:[1,0,1]
	v_pk_add_f32 v[90:91], v[90:91], v[98:99] op_sel:[0,1] op_sel_hi:[1,0]
	v_pk_fma_f32 v[94:95], v[98:99], v[28:29], v[94:95] op_sel:[1,1,0] op_sel_hi:[0,0,1]
	v_pk_add_f32 v[88:89], v[88:89], v[100:101]
	v_pk_fma_f32 v[92:93], v[100:101], v[32:33], v[92:93]
	v_pk_add_f32 v[80:81], v[80:81], v[102:103]
	v_pk_fma_f32 v[84:85], v[102:103], v[40:41], v[84:85]
	v_pk_add_f32 v[96:97], v[46:47], v[36:37] neg_lo:[0,1] neg_hi:[0,1]
	v_pk_add_f32 v[98:99], v[44:45], v[38:39] neg_lo:[0,1] neg_hi:[0,1]
	v_pk_add_f32 v[100:101], v[42:43], v[34:35] op_sel:[1,0] op_sel_hi:[0,1] neg_lo:[0,1] neg_hi:[0,1]
	v_pk_add_f32 v[102:103], v[44:45], v[36:37] op_sel:[1,0] op_sel_hi:[0,1] neg_lo:[0,1] neg_hi:[0,1]
	v_pk_fma_f32 v[96:97], v[96:97], v[96:97], s[26:27] neg_lo:[1,0,0] neg_hi:[1,0,0]
	v_pk_fma_f32 v[98:99], v[98:99], v[98:99], s[26:27] neg_lo:[1,0,0] neg_hi:[1,0,0]
	v_pk_fma_f32 v[100:101], v[100:101], v[100:101], s[24:25] neg_lo:[1,0,0] neg_hi:[1,0,0]
	v_pk_fma_f32 v[102:103], v[102:103], v[102:103], s[24:25] neg_lo:[1,0,0] neg_hi:[1,0,0]
	v_exp_f32_e32 v96, v96
	v_exp_f32_e32 v97, v97
	v_exp_f32_e32 v98, v98
	v_exp_f32_e32 v99, v99
	v_exp_f32_e32 v100, v100
	v_exp_f32_e32 v101, v101
	v_exp_f32_e32 v102, v102
	v_exp_f32_e32 v103, v103
	v_pk_add_f32 v[80:81], v[80:81], v[104:105]
	v_pk_fma_f32 v[84:85], v[104:105], v[42:43], v[84:85]
	v_pk_add_f32 v[88:89], v[88:89], v[104:105]
	v_pk_fma_f32 v[92:93], v[104:105], v[34:35], v[92:93]
	v_pk_add_f32 v[80:81], v[80:81], v[106:107]
	v_pk_fma_f32 v[84:85], v[106:107], v[44:45], v[84:85]
	v_pk_add_f32 v[90:91], v[90:91], v[106:107]
	v_pk_fma_f32 v[94:95], v[106:107], v[34:35], v[94:95]
	v_pk_add_f32 v[82:83], v[82:83], v[108:109]
	v_pk_fma_f32 v[86:87], v[108:109], v[42:43], v[86:87]
	v_pk_add_f32 v[88:89], v[88:89], v[108:109]
	v_pk_fma_f32 v[92:93], v[108:109], v[36:37], v[92:93]
	v_pk_add_f32 v[82:83], v[82:83], v[110:111]
	v_pk_fma_f32 v[86:87], v[110:111], v[44:45], v[86:87]
	v_pk_add_f32 v[90:91], v[90:91], v[110:111]
	v_pk_fma_f32 v[94:95], v[110:111], v[36:37], v[94:95]
	v_pk_add_f32 v[104:105], v[42:43], v[40:41] neg_lo:[0,1] neg_hi:[0,1]
	v_pk_add_f32 v[106:107], v[44:45], v[42:43] neg_lo:[0,1] neg_hi:[0,1]
	v_pk_add_f32 v[108:109], v[46:47], v[44:45] neg_lo:[0,1] neg_hi:[0,1]
	v_pk_fma_f32 v[104:105], v[104:105], v[104:105], s[22:23] neg_lo:[1,0,0] neg_hi:[1,0,0]
	v_pk_fma_f32 v[106:107], v[106:107], v[106:107], s[22:23] neg_lo:[1,0,0] neg_hi:[1,0,0]
	v_pk_fma_f32 v[108:109], v[108:109], v[108:109], s[22:23] neg_lo:[1,0,0] neg_hi:[1,0,0]
	v_exp_f32_e32 v104, v104
	v_exp_f32_e32 v105, v105
	v_exp_f32_e32 v106, v106
	v_exp_f32_e32 v107, v107
	v_exp_f32_e32 v108, v108
	v_exp_f32_e32 v109, v109
	v_pk_add_f32 v[82:83], v[82:83], v[96:97]
	v_pk_fma_f32 v[86:87], v[96:97], v[46:47], v[86:87]
	v_pk_add_f32 v[90:91], v[90:91], v[98:99]
	v_pk_fma_f32 v[94:95], v[98:99], v[38:39], v[94:95]
	v_pk_add_f32 v[80:81], v[80:81], v[100:101]
	v_pk_fma_f32 v[84:85], v[100:101], v[42:43], v[84:85] op_sel:[0,1,0] op_sel_hi:[1,0,1]
	v_pk_add_f32 v[88:89], v[88:89], v[100:101] op_sel:[0,1] op_sel_hi:[1,0]
	v_pk_fma_f32 v[92:93], v[100:101], v[34:35], v[92:93] op_sel:[1,1,0] op_sel_hi:[0,0,1]
	v_pk_add_f32 v[82:83], v[82:83], v[102:103]
	v_pk_fma_f32 v[86:87], v[102:103], v[44:45], v[86:87] op_sel:[0,1,0] op_sel_hi:[1,0,1]
	v_pk_add_f32 v[90:91], v[90:91], v[102:103] op_sel:[0,1] op_sel_hi:[1,0]
	v_pk_fma_f32 v[94:95], v[102:103], v[36:37], v[94:95] op_sel:[1,1,0] op_sel_hi:[0,0,1]
	v_sub_f32_e32 v96, v42, v25
	v_sub_f32_e32 v98, v41, v26
	v_sub_f32_e32 v100, v44, v27
	v_sub_f32_e32 v102, v43, v28
	v_sub_f32_e32 v97, v46, v29
	v_sub_f32_e32 v99, v45, v30
	v_sub_f32_e32 v101, v42, v33
	v_sub_f32_e32 v103, v41, v34
	v_fma_f32 v96, -v96, v96, s26
	v_fma_f32 v98, -v98, v98, s26
	v_fma_f32 v100, -v100, v100, s26
	v_fma_f32 v102, -v102, v102, s26
	v_fma_f32 v97, -v97, v97, s26
	v_fma_f32 v99, -v99, v99, s26
	v_fma_f32 v101, -v101, v101, s24
	v_fma_f32 v103, -v103, v103, s24
	v_exp_f32_e32 v96, v96
	v_exp_f32_e32 v98, v98
	v_exp_f32_e32 v100, v100
	v_exp_f32_e32 v102, v102
	v_exp_f32_e32 v97, v97
	v_exp_f32_e32 v99, v99
	v_exp_f32_e32 v101, v101
	v_exp_f32_e32 v103, v103
	v_pk_add_f32 v[88:89], v[88:89], v[104:105]
	v_pk_fma_f32 v[92:93], v[104:105], v[40:41], v[92:93]
	v_pk_add_f32 v[90:91], v[90:91], v[106:107]
	v_pk_add_f32 v[88:89], v[88:89], v[106:107]
	v_pk_fma_f32 v[92:93], v[106:107], v[44:45], v[92:93]
	v_pk_fma_f32 v[94:95], v[106:107], v[42:43], v[94:95]
	v_pk_add_f32 v[90:91], v[90:91], v[108:109]
	v_pk_fma_f32 v[94:95], v[108:109], v[46:47], v[94:95]
	v_sub_f32_e32 v108, v44, v35
	v_sub_f32_e32 v110, v43, v36
	v_sub_f32_e32 v105, v46, v37
	v_sub_f32_e32 v107, v45, v38
	v_sub_f32_e32 v109, v42, v41
	v_sub_f32_e32 v104, v43, v42
	v_sub_f32_e32 v111, v44, v43
	v_sub_f32_e32 v106, v45, v44
	v_fma_f32 v108, -v108, v108, s24
	v_fma_f32 v110, -v110, v110, s24
	v_fma_f32 v105, -v105, v105, s24
	v_fma_f32 v107, -v107, v107, s24
	v_fma_f32 v109, -v109, v109, s20
	v_fma_f32 v104, -v104, v104, s20
	v_fma_f32 v111, -v111, v111, s20
	v_fma_f32 v106, -v106, v106, s20
	v_exp_f32_e32 v108, v108
	v_exp_f32_e32 v110, v110
	v_exp_f32_e32 v105, v105
	v_exp_f32_e32 v107, v107
	v_exp_f32_e32 v109, v109
	v_exp_f32_e32 v104, v104
	v_exp_f32_e32 v111, v111
	v_exp_f32_e32 v106, v106
	v_add_f32_e32 v88, v88, v96
	v_fmac_f32_e32 v92, v96, v25
	v_add_f32_e32 v72, v72, v98
	v_fmac_f32_e32 v76, v98, v41
	v_add_f32_e32 v73, v73, v100
	v_fmac_f32_e32 v77, v100, v44
	v_add_f32_e32 v90, v90, v100
	v_fmac_f32_e32 v94, v100, v27
	v_add_f32_e32 v74, v74, v102
	v_fmac_f32_e32 v78, v102, v43
	v_add_f32_e32 v89, v89, v102
	v_fmac_f32_e32 v93, v102, v28
	v_add_f32_e32 v75, v75, v97
	v_fmac_f32_e32 v79, v97, v46
	v_add_f32_e32 v91, v91, v99
	v_fmac_f32_e32 v95, v99, v30
	v_add_f32_e32 v88, v88, v101
	v_fmac_f32_e32 v92, v101, v33
	v_add_f32_e32 v80, v80, v103
	v_fmac_f32_e32 v84, v103, v41
	v_sub_f32_e64 v96, v46, v45
	v_fma_f32 v96, -v96, v96, s20
	s_nop 0
	v_exp_f32_e32 v96, v96
	v_add_f32_e32 v81, v81, v108
	v_fmac_f32_e32 v85, v108, v44
	v_add_f32_e32 v90, v90, v108
	v_fmac_f32_e32 v94, v108, v35
	v_add_f32_e32 v82, v82, v110
	v_fmac_f32_e32 v86, v110, v43
	v_add_f32_e32 v89, v89, v110
	v_fmac_f32_e32 v93, v110, v36
	v_add_f32_e32 v83, v83, v105
	v_fmac_f32_e32 v87, v105, v46
	v_add_f32_e32 v91, v91, v107
	v_fmac_f32_e32 v95, v107, v38
	v_add_f32_e32 v88, v88, v109
	v_fmac_f32_e32 v92, v109, v41
	v_add_f32_e32 v89, v89, v111
	v_fmac_f32_e32 v93, v111, v44
	v_add_f32_e32 v90, v90, v111
	v_fmac_f32_e32 v94, v111, v43
	v_pk_add_f32 v[88:89], v[88:89], v[104:105] op_sel_hi:[1,0]
	v_pk_fma_f32 v[92:93], v[104:105], v[42:43], v[92:93] op_sel:[0,1,0] op_sel_hi:[0,0,1]
	v_pk_add_f32 v[90:91], v[90:91], v[106:107] op_sel_hi:[1,0]
	v_pk_fma_f32 v[94:95], v[106:107], v[44:45], v[94:95] op_sel:[0,1,0] op_sel_hi:[0,0,1]
	s_nop 0
	v_add_f32_e32 v91, v91, v96
	v_fmac_f32_e32 v95, v96, v46
	v_rcp_f32_e32 v96, v72
	v_rcp_f32_e32 v97, v73
	v_rcp_f32_e32 v98, v74
	v_rcp_f32_e64 v99, v75
	v_pk_mul_f32 v[76:77], v[76:77], s[34:35]
	v_pk_mul_f32 v[78:79], v[78:79], s[34:35]
	v_pk_mul_f32 v[76:77], v[76:77], v[96:97]
	v_pk_mul_f32 v[78:79], v[78:79], v[98:99]
	buffer_store_dwordx4 v[76:79], v114, s[12:15], 0 offen offset:2048 sc1
	s_waitcnt vmcnt(5)
	s_nop 0
	v_mov_b32_dpp v48, v52 row_shr:1 row_mask:0xf bank_mask:0xf
	v_mov_b32_dpp v49, v53 row_shr:1 row_mask:0xf bank_mask:0xf
	v_mov_b32_dpp v54, v50 row_shl:1 row_mask:0xf bank_mask:0xf
	v_mov_b32_dpp v55, v51 row_shl:1 row_mask:0xf bank_mask:0xf
	v_pk_mul_f32 v[50:51], v[50:51], s[32:33]
	v_pk_mul_f32 v[52:53], v[52:53], s[32:33]
	v_cndmask_b32_e64 v49, v49, v48, vcc
	v_cndmask_b32_e64 v54, v54, v55, s[16:17]
	v_pk_mul_f32 v[48:49], v[48:49], s[32:33]
	v_pk_mul_f32 v[54:55], v[54:55], s[32:33]
	v_pk_add_f32 v[96:97], v[48:49], v[34:35] neg_lo:[0,1] neg_hi:[0,1]
	v_pk_add_f32 v[98:99], v[50:51], v[34:35] neg_lo:[0,1] neg_hi:[0,1]
	v_pk_add_f32 v[100:101], v[52:53], v[34:35] neg_lo:[0,1] neg_hi:[0,1]
	v_pk_add_f32 v[102:103], v[50:51], v[36:37] neg_lo:[0,1] neg_hi:[0,1]
	v_pk_fma_f32 v[96:97], v[96:97], v[96:97], s[28:29] neg_lo:[1,0,0] neg_hi:[1,0,0]
	v_pk_fma_f32 v[98:99], v[98:99], v[98:99], s[22:23] neg_lo:[1,0,0] neg_hi:[1,0,0]
	v_pk_fma_f32 v[100:101], v[100:101], v[100:101], s[28:29] neg_lo:[1,0,0] neg_hi:[1,0,0]
	v_pk_fma_f32 v[102:103], v[102:103], v[102:103], s[28:29] neg_lo:[1,0,0] neg_hi:[1,0,0]
	v_exp_f32_e32 v96, v96
	v_exp_f32_e32 v97, v97
	v_exp_f32_e32 v98, v98
	v_exp_f32_e32 v99, v99
	v_exp_f32_e32 v100, v100
	v_exp_f32_e32 v101, v101
	v_exp_f32_e32 v102, v102
	v_exp_f32_e32 v103, v103
	v_pk_add_f32 v[104:105], v[52:53], v[36:37] neg_lo:[0,1] neg_hi:[0,1]
	v_pk_add_f32 v[106:107], v[54:55], v[36:37] neg_lo:[0,1] neg_hi:[0,1]
	v_pk_add_f32 v[108:109], v[50:51], v[34:35] op_sel:[1,0] op_sel_hi:[0,1] neg_lo:[0,1] neg_hi:[0,1]
	v_pk_add_f32 v[110:111], v[52:53], v[36:37] op_sel:[1,0] op_sel_hi:[0,1] neg_lo:[0,1] neg_hi:[0,1]
	v_pk_fma_f32 v[104:105], v[104:105], v[104:105], s[22:23] neg_lo:[1,0,0] neg_hi:[1,0,0]
	v_pk_fma_f32 v[106:107], v[106:107], v[106:107], s[28:29] neg_lo:[1,0,0] neg_hi:[1,0,0]
	v_pk_fma_f32 v[108:109], v[108:109], v[108:109], s[26:27] neg_lo:[1,0,0] neg_hi:[1,0,0]
	v_pk_fma_f32 v[110:111], v[110:111], v[110:111], s[26:27] neg_lo:[1,0,0] neg_hi:[1,0,0]
	v_exp_f32_e32 v104, v104
	v_exp_f32_e32 v105, v105
	v_exp_f32_e32 v106, v106
	v_exp_f32_e32 v107, v107
	v_exp_f32_e32 v108, v108
	v_exp_f32_e32 v109, v109
	v_exp_f32_e32 v110, v110
	v_exp_f32_e32 v111, v111
	v_pk_add_f32 v[80:81], v[80:81], v[96:97]
	v_pk_fma_f32 v[84:85], v[96:97], v[48:49], v[84:85]
	v_pk_add_f32 v[82:83], v[82:83], v[102:103]
	v_pk_add_f32 v[80:81], v[80:81], v[98:99]
	v_pk_fma_f32 v[84:85], v[98:99], v[50:51], v[84:85]
	v_pk_fma_f32 v[86:87], v[102:103], v[50:51], v[86:87]
	v_pk_add_f32 v[80:81], v[80:81], v[100:101]
	v_pk_fma_f32 v[84:85], v[100:101], v[52:53], v[84:85]
	v_pk_add_f32 v[96:97], v[48:49], v[42:43] neg_lo:[0,1] neg_hi:[0,1]
	v_pk_add_f32 v[98:99], v[50:51], v[42:43] neg_lo:[0,1] neg_hi:[0,1]
	v_pk_add_f32 v[100:101], v[52:53], v[42:43] neg_lo:[0,1] neg_hi:[0,1]
	v_pk_add_f32 v[102:103], v[50:51], v[44:45] neg_lo:[0,1] neg_hi:[0,1]
	v_pk_fma_f32 v[96:97], v[96:97], v[96:97], s[26:27] neg_lo:[1,0,0] neg_hi:[1,0,0]
	v_pk_fma_f32 v[98:99], v[98:99], v[98:99], s[20:21] neg_lo:[1,0,0] neg_hi:[1,0,0]
	v_pk_fma_f32 v[100:101], v[100:101], v[100:101], s[26:27] neg_lo:[1,0,0] neg_hi:[1,0,0]
	v_pk_fma_f32 v[102:103], v[102:103], v[102:103], s[26:27] neg_lo:[1,0,0] neg_hi:[1,0,0]
	v_exp_f32_e32 v96, v96
	v_exp_f32_e32 v97, v97
	v_exp_f32_e32 v98, v98
	v_exp_f32_e32 v99, v99
	v_exp_f32_e32 v100, v100
	v_exp_f32_e32 v101, v101
	v_exp_f32_e32 v102, v102
	v_exp_f32_e32 v103, v103
	v_pk_add_f32 v[82:83], v[82:83], v[104:105]
	v_pk_fma_f32 v[86:87], v[104:105], v[52:53], v[86:87]
	v_pk_add_f32 v[80:81], v[80:81], v[108:109]
	v_pk_add_f32 v[82:83], v[82:83], v[106:107]
	v_pk_fma_f32 v[86:87], v[106:107], v[54:55], v[86:87]
	v_pk_fma_f32 v[84:85], v[108:109], v[50:51], v[84:85] op_sel:[0,1,0] op_sel_hi:[1,0,1]
	v_pk_add_f32 v[82:83], v[82:83], v[110:111]
	v_pk_fma_f32 v[86:87], v[110:111], v[52:53], v[86:87] op_sel:[0,1,0] op_sel_hi:[1,0,1]
	v_pk_add_f32 v[104:105], v[52:53], v[44:45] neg_lo:[0,1] neg_hi:[0,1]
	v_pk_add_f32 v[106:107], v[54:55], v[44:45] neg_lo:[0,1] neg_hi:[0,1]
	v_pk_add_f32 v[108:109], v[50:51], v[42:43] op_sel:[1,0] op_sel_hi:[0,1] neg_lo:[0,1] neg_hi:[0,1]
	v_pk_add_f32 v[110:111], v[52:53], v[44:45] op_sel:[1,0] op_sel_hi:[0,1] neg_lo:[0,1] neg_hi:[0,1]
	v_pk_fma_f32 v[104:105], v[104:105], v[104:105], s[20:21] neg_lo:[1,0,0] neg_hi:[1,0,0]
	v_pk_fma_f32 v[106:107], v[106:107], v[106:107], s[26:27] neg_lo:[1,0,0] neg_hi:[1,0,0]
	v_pk_fma_f32 v[108:109], v[108:109], v[108:109], s[24:25] neg_lo:[1,0,0] neg_hi:[1,0,0]
	v_pk_fma_f32 v[110:111], v[110:111], v[110:111], s[24:25] neg_lo:[1,0,0] neg_hi:[1,0,0]
	v_exp_f32_e32 v104, v104
	v_exp_f32_e32 v105, v105
	v_exp_f32_e32 v106, v106
	v_exp_f32_e32 v107, v107
	v_exp_f32_e32 v108, v108
	v_exp_f32_e32 v109, v109
	v_exp_f32_e32 v110, v110
	v_exp_f32_e32 v111, v111
	v_pk_add_f32 v[88:89], v[88:89], v[96:97]
	v_pk_fma_f32 v[92:93], v[96:97], v[48:49], v[92:93]
	v_pk_add_f32 v[90:91], v[90:91], v[102:103]
	v_pk_add_f32 v[88:89], v[88:89], v[98:99]
	v_pk_fma_f32 v[92:93], v[98:99], v[50:51], v[92:93]
	v_pk_fma_f32 v[94:95], v[102:103], v[50:51], v[94:95]
	v_pk_add_f32 v[88:89], v[88:89], v[100:101]
	v_pk_fma_f32 v[92:93], v[100:101], v[52:53], v[92:93]
	v_sub_f32_e32 v96, v49, v34
	v_sub_f32_e32 v98, v52, v35
	v_sub_f32_e32 v100, v51, v36
	v_sub_f32_e32 v102, v54, v37
	v_sub_f32_e32 v97, v49, v42
	v_sub_f32_e32 v99, v52, v43
	v_sub_f32_e32 v101, v51, v44
	v_sub_f32_e32 v103, v54, v45
	v_fma_f32 v96, -v96, v96, s26
	v_fma_f32 v98, -v98, v98, s26
	v_fma_f32 v100, -v100, v100, s26
	v_fma_f32 v102, -v102, v102, s26
	v_fma_f32 v97, -v97, v97, s24
	v_fma_f32 v99, -v99, v99, s24
	v_fma_f32 v101, -v101, v101, s24
	v_fma_f32 v103, -v103, v103, s24
	v_exp_f32_e32 v96, v96
	v_exp_f32_e32 v98, v98
	v_exp_f32_e32 v100, v100
	v_exp_f32_e32 v102, v102
	v_exp_f32_e32 v97, v97
	v_exp_f32_e32 v99, v99
	v_exp_f32_e32 v101, v101
	v_exp_f32_e32 v103, v103
	v_pk_add_f32 v[90:91], v[90:91], v[104:105]
	v_pk_fma_f32 v[94:95], v[104:105], v[52:53], v[94:95]
	v_pk_add_f32 v[88:89], v[88:89], v[108:109]
	v_pk_add_f32 v[90:91], v[90:91], v[106:107]
	v_pk_fma_f32 v[94:95], v[106:107], v[54:55], v[94:95]
	v_pk_fma_f32 v[92:93], v[108:109], v[50:51], v[92:93] op_sel:[0,1,0] op_sel_hi:[1,0,1]
	v_pk_add_f32 v[90:91], v[90:91], v[110:111]
	v_pk_fma_f32 v[94:95], v[110:111], v[52:53], v[94:95] op_sel:[0,1,0] op_sel_hi:[1,0,1]
	v_add_f32_e32 v80, v80, v96
	v_fmac_f32_e32 v84, v96, v49
	v_add_f32_e32 v81, v81, v98
	v_fmac_f32_e32 v85, v98, v52
	v_add_f32_e32 v82, v82, v100
	v_fmac_f32_e32 v86, v100, v51
	v_add_f32_e32 v83, v83, v102
	v_fmac_f32_e32 v87, v102, v54
	v_add_f32_e32 v88, v88, v97
	v_fmac_f32_e32 v92, v97, v49
	v_add_f32_e32 v89, v89, v99
	v_fmac_f32_e32 v93, v99, v52
	v_add_f32_e32 v90, v90, v101
	v_fmac_f32_e32 v94, v101, v51
	v_add_f32_e32 v91, v91, v103
	v_fmac_f32_e32 v95, v103, v54
	v_rcp_f32_e32 v96, v80
	v_rcp_f32_e32 v97, v81
	v_rcp_f32_e32 v98, v82
	v_rcp_f32_e32 v99, v83
	v_pk_mul_f32 v[84:85], v[84:85], s[34:35]
	v_pk_mul_f32 v[86:87], v[86:87], s[34:35]
	v_pk_mul_f32 v[84:85], v[84:85], v[96:97]
	v_pk_mul_f32 v[86:87], v[86:87], v[98:99]
	buffer_store_dwordx4 v[84:87], v119, s[12:15], 0 offen sc1
	s_waitcnt vmcnt(3)
	s_nop 0
	v_mov_b32_dpp v56, v60 row_shr:1 row_mask:0xf bank_mask:0xf
	v_mov_b32_dpp v57, v61 row_shr:1 row_mask:0xf bank_mask:0xf
	v_mov_b32_dpp v62, v58 row_shl:1 row_mask:0xf bank_mask:0xf
	v_mov_b32_dpp v63, v59 row_shl:1 row_mask:0xf bank_mask:0xf
	v_pk_mul_f32 v[58:59], v[58:59], s[32:33]
	v_pk_mul_f32 v[60:61], v[60:61], s[32:33]
	v_cndmask_b32_e64 v57, v57, v56, vcc
	v_cndmask_b32_e64 v62, v62, v63, s[16:17]
	v_pk_mul_f32 v[56:57], v[56:57], s[32:33]
	v_pk_mul_f32 v[62:63], v[62:63], s[32:33]
	v_pk_add_f32 v[96:97], v[56:57], v[42:43] neg_lo:[0,1] neg_hi:[0,1]
	v_pk_add_f32 v[98:99], v[58:59], v[42:43] neg_lo:[0,1] neg_hi:[0,1]
	v_pk_add_f32 v[100:101], v[60:61], v[42:43] neg_lo:[0,1] neg_hi:[0,1]
	v_pk_add_f32 v[102:103], v[58:59], v[44:45] neg_lo:[0,1] neg_hi:[0,1]
	v_pk_fma_f32 v[96:97], v[96:97], v[96:97], s[28:29] neg_lo:[1,0,0] neg_hi:[1,0,0]
	v_pk_fma_f32 v[98:99], v[98:99], v[98:99], s[22:23] neg_lo:[1,0,0] neg_hi:[1,0,0]
	v_pk_fma_f32 v[100:101], v[100:101], v[100:101], s[28:29] neg_lo:[1,0,0] neg_hi:[1,0,0]
	v_pk_fma_f32 v[102:103], v[102:103], v[102:103], s[28:29] neg_lo:[1,0,0] neg_hi:[1,0,0]
	v_exp_f32_e32 v96, v96
	v_exp_f32_e32 v97, v97
	v_exp_f32_e32 v98, v98
	v_exp_f32_e32 v99, v99
	v_exp_f32_e32 v100, v100
	v_exp_f32_e32 v101, v101
	v_exp_f32_e32 v102, v102
	v_exp_f32_e32 v103, v103
	v_pk_add_f32 v[104:105], v[60:61], v[44:45] neg_lo:[0,1] neg_hi:[0,1]
	v_pk_add_f32 v[106:107], v[62:63], v[44:45] neg_lo:[0,1] neg_hi:[0,1]
	v_pk_add_f32 v[108:109], v[58:59], v[42:43] op_sel:[1,0] op_sel_hi:[0,1] neg_lo:[0,1] neg_hi:[0,1]
	v_pk_add_f32 v[110:111], v[60:61], v[44:45] op_sel:[1,0] op_sel_hi:[0,1] neg_lo:[0,1] neg_hi:[0,1]
	v_pk_fma_f32 v[104:105], v[104:105], v[104:105], s[22:23] neg_lo:[1,0,0] neg_hi:[1,0,0]
	v_pk_fma_f32 v[106:107], v[106:107], v[106:107], s[28:29] neg_lo:[1,0,0] neg_hi:[1,0,0]
	v_pk_fma_f32 v[108:109], v[108:109], v[108:109], s[26:27] neg_lo:[1,0,0] neg_hi:[1,0,0]
	v_pk_fma_f32 v[110:111], v[110:111], v[110:111], s[26:27] neg_lo:[1,0,0] neg_hi:[1,0,0]
	v_exp_f32_e32 v104, v104
	v_exp_f32_e32 v105, v105
	v_exp_f32_e32 v106, v106
	v_exp_f32_e32 v107, v107
	v_exp_f32_e32 v108, v108
	v_exp_f32_e32 v109, v109
	v_exp_f32_e32 v110, v110
	v_exp_f32_e32 v111, v111
	v_pk_add_f32 v[88:89], v[88:89], v[96:97]
	v_pk_fma_f32 v[92:93], v[96:97], v[56:57], v[92:93]
	v_pk_add_f32 v[90:91], v[90:91], v[102:103]
	v_pk_add_f32 v[88:89], v[88:89], v[98:99]
	v_pk_fma_f32 v[92:93], v[98:99], v[58:59], v[92:93]
	v_pk_fma_f32 v[94:95], v[102:103], v[58:59], v[94:95]
	v_pk_add_f32 v[88:89], v[88:89], v[100:101]
	v_pk_fma_f32 v[92:93], v[100:101], v[60:61], v[92:93]
	v_sub_f32_e32 v96, v57, v42
	v_sub_f32_e32 v98, v60, v43
	v_sub_f32_e32 v100, v59, v44
	v_sub_f32_e32 v102, v62, v45
	v_fma_f32 v96, -v96, v96, s26
	v_fma_f32 v98, -v98, v98, s26
	v_fma_f32 v100, -v100, v100, s26
	v_fma_f32 v102, -v102, v102, s26
	v_exp_f32_e32 v96, v96
	v_exp_f32_e32 v98, v98
	v_exp_f32_e32 v100, v100
	v_exp_f32_e32 v102, v102
	v_pk_add_f32 v[90:91], v[90:91], v[104:105]
	v_pk_fma_f32 v[94:95], v[104:105], v[60:61], v[94:95]
	v_pk_add_f32 v[88:89], v[88:89], v[108:109]
	v_pk_add_f32 v[90:91], v[90:91], v[106:107]
	v_pk_fma_f32 v[94:95], v[106:107], v[62:63], v[94:95]
	v_pk_fma_f32 v[92:93], v[108:109], v[58:59], v[92:93] op_sel:[0,1,0] op_sel_hi:[1,0,1]
	v_pk_add_f32 v[90:91], v[90:91], v[110:111]
	v_pk_fma_f32 v[94:95], v[110:111], v[60:61], v[94:95] op_sel:[0,1,0] op_sel_hi:[1,0,1]
	v_add_f32_e32 v88, v88, v96
	v_fmac_f32_e32 v92, v96, v57
	v_add_f32_e32 v89, v89, v98
	v_fmac_f32_e32 v93, v98, v60
	v_add_f32_e32 v90, v90, v100
	v_fmac_f32_e32 v94, v100, v59
	v_add_f32_e32 v91, v91, v102
	v_fmac_f32_e32 v95, v102, v62
	v_rcp_f32_e32 v96, v88
	v_rcp_f32_e32 v97, v89
	v_rcp_f32_e32 v98, v90
	v_rcp_f32_e32 v99, v91
	v_pk_mul_f32 v[92:93], v[92:93], s[34:35]
	v_pk_mul_f32 v[94:95], v[94:95], s[34:35]
	v_pk_mul_f32 v[92:93], v[92:93], v[96:97]
	v_pk_mul_f32 v[94:95], v[94:95], v[98:99]
	buffer_store_dwordx4 v[92:95], v119, s[12:15], 0 offen offset:2048 sc1
	s_endpgm
